# four-waves-per-row version with a 5-deep load ring per wave (20 KB in flight per block instead of 40 KB)
# baseline (speedup 1.0000x reference)
.Lsc_m3:
	v_mov_b32_e32 v4, v2
	s_cmp_lg_u32 s55, 3
	s_cbranch_scc1 .Lsc_m4
	s_add_i32 s41, s47, 3
	v_min_u32_e32 v4, s41, v3
	v_lshlrev_b32_e32 v4, 4, v4

.Lsc_go:
	s_mov_b32 s42, 0
	s_waitcnt vmcnt(4)
	v_or3_b32 v12, v100, v101, v102
	v_bitop3_b32 v12, v12, s9, v103 bitop3:0xc8
	v_cmp_ne_u32_e32 vcc, 0, v12
	s_and_b64 vcc, vcc, s[48:49]
	s_cbranch_vccz .Lsc_s0
	s_bcnt1_i32_b64 s40, vcc
	v_mbcnt_lo_u32_b32 v13, vcc_lo, 0
	v_mbcnt_hi_u32_b32 v13, vcc_hi, v13
	v_add_u32_e32 v13, s42, v13
	s_add_i32 s42, s42, s40
	v_cmp_gt_i32_e64 s[0:1], s7, v13
	s_and_b64 s[4:5], vcc, s[0:1]
	s_and_saveexec_b64 s[0:1], s[4:5]
	v_lshl_add_u32 v14, v13, 4, v9
	v_lshl_add_u32 v15, v13, 2, v10
	v_mov_b32_e32 v13, v8
	ds_write_b128 v14, v[100:103]
	ds_write_b32 v15, v13
	s_mov_b64 exec, -1
.Lsc_s0:
	s_add_u32 s40, s38, 0x1400
	buffer_load_dwordx4 v[100:103], v2, s[28:31], s40 offen nt
	s_waitcnt vmcnt(4)
	v_or3_b32 v12, v104, v105, v106
	v_bitop3_b32 v12, v12, s9, v107 bitop3:0xc8
	v_cmp_ne_u32_e32 vcc, 0, v12
	s_cbranch_vccz .Lsc_s1
	s_bcnt1_i32_b64 s40, vcc
	v_mbcnt_lo_u32_b32 v13, vcc_lo, 0
	v_mbcnt_hi_u32_b32 v13, vcc_hi, v13
	v_add_u32_e32 v13, s42, v13
	s_add_i32 s42, s42, s40
	v_cmp_gt_i32_e64 s[0:1], s7, v13
	s_and_b64 s[4:5], vcc, s[0:1]
	s_and_saveexec_b64 s[0:1], s[4:5]
	v_lshl_add_u32 v14, v13, 4, v9
	v_lshl_add_u32 v15, v13, 2, v10
	v_add_u32_e32 v13, 0x100, v8
	ds_write_b128 v14, v[104:107]
	ds_write_b32 v15, v13
	s_mov_b64 exec, -1
.Lsc_s1:
	s_add_u32 s40, s38, 0x1800
	buffer_load_dwordx4 v[104:107], v2, s[28:31], s40 offen nt
	s_waitcnt vmcnt(4)
	v_or3_b32 v12, v108, v109, v110
	v_bitop3_b32 v12, v12, s9, v111 bitop3:0xc8
	v_cmp_ne_u32_e32 vcc, 0, v12
	s_cbranch_vccz .Lsc_s2
	s_bcnt1_i32_b64 s40, vcc
	v_mbcnt_lo_u32_b32 v13, vcc_lo, 0
	v_mbcnt_hi_u32_b32 v13, vcc_hi, v13
	v_add_u32_e32 v13, s42, v13
	s_add_i32 s42, s42, s40
	v_cmp_gt_i32_e64 s[0:1], s7, v13
	s_and_b64 s[4:5], vcc, s[0:1]
	s_and_saveexec_b64 s[0:1], s[4:5]
	v_lshl_add_u32 v14, v13, 4, v9
	v_lshl_add_u32 v15, v13, 2, v10
	v_add_u32_e32 v13, 0x200, v8
	ds_write_b128 v14, v[108:111]
	ds_write_b32 v15, v13
	s_mov_b64 exec, -1
.Lsc_s2:
	s_add_u32 s40, s38, 0x1c00
	buffer_load_dwordx4 v[108:111], v2, s[28:31], s40 offen nt
	s_waitcnt vmcnt(4)
	v_or3_b32 v12, v112, v113, v114
	v_bitop3_b32 v12, v12, s9, v115 bitop3:0xc8
	v_cmp_ne_u32_e32 vcc, 0, v12
	s_cbranch_vccz .Lsc_s3
	s_bcnt1_i32_b64 s40, vcc
	v_mbcnt_lo_u32_b32 v13, vcc_lo, 0
	v_mbcnt_hi_u32_b32 v13, vcc_hi, v13
	v_add_u32_e32 v13, s42, v13
	s_add_i32 s42, s42, s40
	v_cmp_gt_i32_e64 s[0:1], s7, v13
	s_and_b64 s[4:5], vcc, s[0:1]
	s_and_saveexec_b64 s[0:1], s[4:5]
	v_lshl_add_u32 v14, v13, 4, v9
	v_lshl_add_u32 v15, v13, 2, v10
	v_add_u32_e32 v13, 0x300, v8
	ds_write_b128 v14, v[112:115]
	ds_write_b32 v15, v13
	s_mov_b64 exec, -1
.Lsc_s3:
	s_add_u32 s40, s38, 0x2000
	buffer_load_dwordx4 v[112:115], v2, s[28:31], s40 offen nt
	s_waitcnt vmcnt(4)
	v_or3_b32 v12, v116, v117, v118
	v_bitop3_b32 v12, v12, s9, v119 bitop3:0xc8
	v_cmp_ne_u32_e32 vcc, 0, v12
	s_cbranch_vccz .Lsc_s4
	s_bcnt1_i32_b64 s40, vcc
	v_mbcnt_lo_u32_b32 v13, vcc_lo, 0
	v_mbcnt_hi_u32_b32 v13, vcc_hi, v13
	v_add_u32_e32 v13, s42, v13
	s_add_i32 s42, s42, s40
	v_cmp_gt_i32_e64 s[0:1], s7, v13
	s_and_b64 s[4:5], vcc, s[0:1]
	s_and_saveexec_b64 s[0:1], s[4:5]
	v_lshl_add_u32 v14, v13, 4, v9
	v_lshl_add_u32 v15, v13, 2, v10
	v_add_u32_e32 v13, 0x400, v8
	ds_write_b128 v14, v[116:119]
	ds_write_b32 v15, v13
	s_mov_b64 exec, -1
.Lsc_s4:
	s_add_u32 s40, s38, 0x2400
	buffer_load_dwordx4 v[116:119], v4, s[28:31], s40 offen nt
	s_waitcnt vmcnt(4)
	v_or3_b32 v12, v100, v101, v102
	v_bitop3_b32 v12, v12, s9, v103 bitop3:0xc8
	v_cmp_ne_u32_e32 vcc, 0, v12
	s_cbranch_vccz .Lsc_s5
	s_bcnt1_i32_b64 s40, vcc
	v_mbcnt_lo_u32_b32 v13, vcc_lo, 0
	v_mbcnt_hi_u32_b32 v13, vcc_hi, v13
	v_add_u32_e32 v13, s42, v13
	s_add_i32 s42, s42, s40
	v_cmp_gt_i32_e64 s[0:1], s7, v13
	s_and_b64 s[4:5], vcc, s[0:1]
	s_and_saveexec_b64 s[0:1], s[4:5]
	v_lshl_add_u32 v14, v13, 4, v9
	v_lshl_add_u32 v15, v13, 2, v10
	v_add_u32_e32 v13, 0x500, v8
	ds_write_b128 v14, v[100:103]
	ds_write_b32 v15, v13
	s_mov_b64 exec, -1
.Lsc_s5:
	s_mov_b32 s40, s39
	buffer_load_dwordx4 v[100:103], v5, s[28:31], s40 offen nt
	s_waitcnt vmcnt(4)
	v_or3_b32 v12, v104, v105, v106
	v_bitop3_b32 v12, v12, s9, v107 bitop3:0xc8
	v_cmp_ne_u32_e32 vcc, 0, v12
	s_cbranch_vccz .Lsc_s6
	s_bcnt1_i32_b64 s40, vcc
	v_mbcnt_lo_u32_b32 v13, vcc_lo, 0
	v_mbcnt_hi_u32_b32 v13, vcc_hi, v13
	v_add_u32_e32 v13, s42, v13
	s_add_i32 s42, s42, s40
	v_cmp_gt_i32_e64 s[0:1], s7, v13
	s_and_b64 s[4:5], vcc, s[0:1]
	s_and_saveexec_b64 s[0:1], s[4:5]
	v_lshl_add_u32 v14, v13, 4, v9
	v_lshl_add_u32 v15, v13, 2, v10
	v_add_u32_e32 v13, 0x600, v8
	ds_write_b128 v14, v[104:107]
	ds_write_b32 v15, v13
	s_mov_b64 exec, -1
.Lsc_s6:
	s_add_u32 s40, s39, 0x400
	buffer_load_dwordx4 v[104:107], v6, s[28:31], s40 offen nt
	s_waitcnt vmcnt(4)
	v_or3_b32 v12, v108, v109, v110
	v_bitop3_b32 v12, v12, s9, v111 bitop3:0xc8
	v_cmp_ne_u32_e32 vcc, 0, v12
	s_cbranch_vccz .Lsc_s7
	s_bcnt1_i32_b64 s40, vcc
	v_mbcnt_lo_u32_b32 v13, vcc_lo, 0
	v_mbcnt_hi_u32_b32 v13, vcc_hi, v13
	v_add_u32_e32 v13, s42, v13
	s_add_i32 s42, s42, s40
	v_cmp_gt_i32_e64 s[0:1], s7, v13
	s_and_b64 s[4:5], vcc, s[0:1]
	s_and_saveexec_b64 s[0:1], s[4:5]
	v_lshl_add_u32 v14, v13, 4, v9
	v_lshl_add_u32 v15, v13, 2, v10
	v_add_u32_e32 v13, 0x700, v8
	ds_write_b128 v14, v[108:111]
	ds_write_b32 v15, v13
	s_mov_b64 exec, -1
.Lsc_s7:
	s_add_u32 s40, s39, 0x800
	buffer_load_dwordx4 v[108:111], v6, s[28:31], s40 offen nt
	s_waitcnt vmcnt(4)
	v_or3_b32 v12, v112, v113, v114
	v_bitop3_b32 v12, v12, s9, v115 bitop3:0xc8
	v_cmp_ne_u32_e32 vcc, 0, v12
	s_cbranch_vccz .Lsc_s8
	s_bcnt1_i32_b64 s40, vcc
	v_mbcnt_lo_u32_b32 v13, vcc_lo, 0
	v_mbcnt_hi_u32_b32 v13, vcc_hi, v13
	v_add_u32_e32 v13, s42, v13
	s_add_i32 s42, s42, s40
	v_cmp_gt_i32_e64 s[0:1], s7, v13
	s_and_b64 s[4:5], vcc, s[0:1]
	s_and_saveexec_b64 s[0:1], s[4:5]
	v_lshl_add_u32 v14, v13, 4, v9
	v_lshl_add_u32 v15, v13, 2, v10
	v_add_u32_e32 v13, 0x800, v8
	ds_write_b128 v14, v[112:115]
	ds_write_b32 v15, v13
	s_mov_b64 exec, -1
.Lsc_s8:
	s_add_u32 s40, s39, 0xc00
	buffer_load_dwordx4 v[112:115], v6, s[28:31], s40 offen nt
	s_waitcnt vmcnt(4)
	v_or3_b32 v12, v116, v117, v118
	v_bitop3_b32 v12, v12, s9, v119 bitop3:0xc8
	v_cmp_ne_u32_e32 vcc, 0, v12
	s_and_b64 vcc, vcc, s[50:51]
	s_cbranch_vccz .Lsc_s9
	s_bcnt1_i32_b64 s40, vcc
	v_mbcnt_lo_u32_b32 v13, vcc_lo, 0
	v_mbcnt_hi_u32_b32 v13, vcc_hi, v13
	v_add_u32_e32 v13, s42, v13
	s_add_i32 s42, s42, s40
	v_cmp_gt_i32_e64 s[0:1], s7, v13
	s_and_b64 s[4:5], vcc, s[0:1]
	s_and_saveexec_b64 s[0:1], s[4:5]
	v_lshl_add_u32 v14, v13, 4, v9
	v_lshl_add_u32 v15, v13, 2, v10
	v_add_u32_e32 v13, 0x900, v8
	ds_write_b128 v14, v[116:119]
	ds_write_b32 v15, v13
	s_mov_b64 exec, -1
.Lsc_s9:
	s_add_u32 s40, s39, 0x1000
	buffer_load_dwordx4 v[116:119], v6, s[28:31], s40 offen nt
	s_waitcnt lgkmcnt(0)
	s_add_i32 s42, s42, 1
	v_mov_b32_e32 v12, s42
	ds_write_b32 v11, v12
	s_cmp_eq_u32 s35, s36
	s_cbranch_scc1 .LBB1_384
	s_add_i32 s35, s35, 1
	s_mov_b32 s37, s52
	s_mov_b32 s38, s39
	s_mov_b32 s47, s53
	s_branch .Lsc_row
